# v30 + e2f moved into gather shadow + speculative E-row prefetch after screening argmin
# baseline (speedup 1.0000x reference)
.Lfront_nocursor:
	s_waitcnt lgkmcnt(0)
	s_barrier
	s_mov_b64 exec, s[36:37]
	ds_add_rtn_u32 v106, v74, v143 offset:64
	s_mov_b64 exec, s[38:39]
	ds_add_rtn_u32 v107, v75, v143 offset:64
	s_mov_b64 exec, s[40:41]
	ds_add_rtn_u32 v108, v76, v143 offset:64
	s_mov_b64 exec, s[42:43]
	ds_add_rtn_u32 v109, v77, v143 offset:64
	s_mov_b64 exec, s[44:45]
	ds_add_rtn_u32 v110, v78, v143 offset:64
	s_mov_b64 exec, s[46:47]
	ds_add_rtn_u32 v111, v79, v143 offset:64
	s_mov_b64 exec, s[48:49]
	ds_add_rtn_u32 v112, v80, v143 offset:64
	s_mov_b64 exec, s[50:51]
	ds_add_rtn_u32 v113, v81, v143 offset:64
	s_mov_b64 exec, s[52:53]
	ds_add_rtn_u32 v114, v82, v143 offset:64
	s_mov_b64 exec, s[54:55]
	ds_add_rtn_u32 v115, v83, v143 offset:64
	s_mov_b64 exec, s[56:57]
	ds_add_rtn_u32 v116, v84, v143 offset:64
	s_mov_b64 exec, s[58:59]
	ds_add_rtn_u32 v117, v85, v143 offset:64
	s_mov_b64 exec, s[60:61]
	ds_add_rtn_u32 v118, v86, v143 offset:64
	s_mov_b64 exec, s[62:63]
	ds_add_rtn_u32 v119, v87, v143 offset:64
	s_mov_b64 exec, s[64:65]
	ds_add_rtn_u32 v120, v88, v143 offset:64
	s_mov_b64 exec, s[66:67]
	ds_add_rtn_u32 v121, v89, v143 offset:64
	s_mov_b64 exec, s[68:69]
	ds_add_rtn_u32 v122, v90, v143 offset:64
	s_mov_b64 exec, s[70:71]
	ds_add_rtn_u32 v123, v91, v143 offset:64
	s_mov_b64 exec, s[72:73]
	ds_add_rtn_u32 v124, v92, v143 offset:64
	s_mov_b64 exec, s[74:75]
	ds_add_rtn_u32 v125, v93, v143 offset:64
	s_mov_b64 exec, s[76:77]
	ds_add_rtn_u32 v126, v94, v143 offset:64
	s_mov_b64 exec, s[78:79]
	ds_add_rtn_u32 v127, v95, v143 offset:64
	s_mov_b64 exec, s[80:81]
	ds_add_rtn_u32 v128, v96, v143 offset:64
	s_mov_b64 exec, s[82:83]
	ds_add_rtn_u32 v129, v97, v143 offset:64
	s_mov_b64 exec, s[84:85]
	ds_add_rtn_u32 v130, v98, v143 offset:64
	s_mov_b64 exec, s[86:87]
	ds_add_rtn_u32 v131, v99, v143 offset:64
	s_mov_b64 exec, s[88:89]
	ds_add_rtn_u32 v132, v100, v143 offset:64
	s_mov_b64 exec, s[90:91]
	ds_add_rtn_u32 v133, v101, v143 offset:64
	s_mov_b64 exec, s[92:93]
	ds_add_rtn_u32 v134, v102, v143 offset:64
	s_mov_b64 exec, s[94:95]
	ds_add_rtn_u32 v135, v103, v143 offset:64
	s_mov_b64 exec, s[96:97]
	ds_add_rtn_u32 v136, v104, v143 offset:64
	s_mov_b64 exec, s[98:99]
	ds_add_rtn_u32 v137, v105, v143 offset:64
	s_mov_b64 exec, -1
	v_add_u32_e32 v146, 0x0, v145
	v_and_or_b32 v146, v74, 60, v146
	s_waitcnt lgkmcnt(0)
	s_mov_b64 exec, s[36:37]
	ds_write_b32 v106, v146
	s_mov_b64 exec, -1
	v_add_u32_e32 v147, 0x40, v145
	v_and_or_b32 v147, v75, 60, v147
	s_mov_b64 exec, s[38:39]
	ds_write_b32 v107, v147
	s_mov_b64 exec, -1
	v_add_u32_e32 v146, 0x80, v145
	v_and_or_b32 v146, v76, 60, v146
	s_mov_b64 exec, s[40:41]
	ds_write_b32 v108, v146
	s_mov_b64 exec, -1
	v_add_u32_e32 v147, 0xc0, v145
	v_and_or_b32 v147, v77, 60, v147
	s_mov_b64 exec, s[42:43]
	ds_write_b32 v109, v147
	s_mov_b64 exec, -1
	v_add_u32_e32 v146, 0x10000, v145
	v_and_or_b32 v146, v78, 60, v146
	s_mov_b64 exec, s[44:45]
	ds_write_b32 v110, v146
	s_mov_b64 exec, -1
	v_add_u32_e32 v147, 0x10040, v145
	v_and_or_b32 v147, v79, 60, v147
	s_mov_b64 exec, s[46:47]
	ds_write_b32 v111, v147
	s_mov_b64 exec, -1
	v_add_u32_e32 v146, 0x10080, v145
	v_and_or_b32 v146, v80, 60, v146
	s_mov_b64 exec, s[48:49]
	ds_write_b32 v112, v146
	s_mov_b64 exec, -1
	v_add_u32_e32 v147, 0x100c0, v145
	v_and_or_b32 v147, v81, 60, v147
	s_mov_b64 exec, s[50:51]
	ds_write_b32 v113, v147
	s_mov_b64 exec, -1
	v_add_u32_e32 v146, 0x20000, v145
	v_and_or_b32 v146, v82, 60, v146
	s_mov_b64 exec, s[52:53]
	ds_write_b32 v114, v146
	s_mov_b64 exec, -1
	v_add_u32_e32 v147, 0x20040, v145
	v_and_or_b32 v147, v83, 60, v147
	s_mov_b64 exec, s[54:55]
	ds_write_b32 v115, v147
	s_mov_b64 exec, -1
	v_add_u32_e32 v146, 0x20080, v145
	v_and_or_b32 v146, v84, 60, v146
	s_mov_b64 exec, s[56:57]
	ds_write_b32 v116, v146
	s_mov_b64 exec, -1
	v_add_u32_e32 v147, 0x200c0, v145
	v_and_or_b32 v147, v85, 60, v147
	s_mov_b64 exec, s[58:59]
	ds_write_b32 v117, v147
	s_mov_b64 exec, -1
	v_add_u32_e32 v146, 0x30000, v145
	v_and_or_b32 v146, v86, 60, v146
	s_mov_b64 exec, s[60:61]
	ds_write_b32 v118, v146
	s_mov_b64 exec, -1
	v_add_u32_e32 v147, 0x30040, v145
	v_and_or_b32 v147, v87, 60, v147
	s_mov_b64 exec, s[62:63]
	ds_write_b32 v119, v147
	s_mov_b64 exec, -1
	v_add_u32_e32 v146, 0x30080, v145
	v_and_or_b32 v146, v88, 60, v146
	s_mov_b64 exec, s[64:65]
	ds_write_b32 v120, v146
	s_mov_b64 exec, -1
	v_add_u32_e32 v147, 0x300c0, v145
	v_and_or_b32 v147, v89, 60, v147
	s_mov_b64 exec, s[66:67]
	ds_write_b32 v121, v147
	s_mov_b64 exec, -1
	v_add_u32_e32 v146, 0x40000, v145
	v_and_or_b32 v146, v90, 60, v146
	s_mov_b64 exec, s[68:69]
	ds_write_b32 v122, v146
	s_mov_b64 exec, -1
	v_add_u32_e32 v147, 0x40040, v145
	v_and_or_b32 v147, v91, 60, v147
	s_mov_b64 exec, s[70:71]
	ds_write_b32 v123, v147
	s_mov_b64 exec, -1
	v_add_u32_e32 v146, 0x40080, v145
	v_and_or_b32 v146, v92, 60, v146
	s_mov_b64 exec, s[72:73]
	ds_write_b32 v124, v146
	s_mov_b64 exec, -1
	v_add_u32_e32 v147, 0x400c0, v145
	v_and_or_b32 v147, v93, 60, v147
	s_mov_b64 exec, s[74:75]
	ds_write_b32 v125, v147
	s_mov_b64 exec, -1
	v_add_u32_e32 v146, 0x50000, v145
	v_and_or_b32 v146, v94, 60, v146
	s_mov_b64 exec, s[76:77]
	ds_write_b32 v126, v146
	s_mov_b64 exec, -1
	v_add_u32_e32 v147, 0x50040, v145
	v_and_or_b32 v147, v95, 60, v147
	s_mov_b64 exec, s[78:79]
	ds_write_b32 v127, v147
	s_mov_b64 exec, -1
	v_add_u32_e32 v146, 0x50080, v145
	v_and_or_b32 v146, v96, 60, v146
	s_mov_b64 exec, s[80:81]
	ds_write_b32 v128, v146
	s_mov_b64 exec, -1
	v_add_u32_e32 v147, 0x500c0, v145
	v_and_or_b32 v147, v97, 60, v147
	s_mov_b64 exec, s[82:83]
	ds_write_b32 v129, v147
	s_mov_b64 exec, -1
	v_add_u32_e32 v146, 0x60000, v145
	v_and_or_b32 v146, v98, 60, v146
	s_mov_b64 exec, s[84:85]
	ds_write_b32 v130, v146
	s_mov_b64 exec, -1
	v_add_u32_e32 v147, 0x60040, v145
	v_and_or_b32 v147, v99, 60, v147
	s_mov_b64 exec, s[86:87]
	ds_write_b32 v131, v147
	s_mov_b64 exec, -1
	v_add_u32_e32 v146, 0x60080, v145
	v_and_or_b32 v146, v100, 60, v146
	s_mov_b64 exec, s[88:89]
	ds_write_b32 v132, v146
	s_mov_b64 exec, -1
	v_add_u32_e32 v147, 0x600c0, v145
	v_and_or_b32 v147, v101, 60, v147
	s_mov_b64 exec, s[90:91]
	ds_write_b32 v133, v147
	s_mov_b64 exec, -1
	v_add_u32_e32 v146, 0x70000, v145
	v_and_or_b32 v146, v102, 60, v146
	s_mov_b64 exec, s[92:93]
	ds_write_b32 v134, v146
	s_mov_b64 exec, -1
	v_add_u32_e32 v147, 0x70040, v145
	v_and_or_b32 v147, v103, 60, v147
	s_mov_b64 exec, s[94:95]
	ds_write_b32 v135, v147
	s_mov_b64 exec, -1
	v_add_u32_e32 v146, 0x70080, v145
	v_and_or_b32 v146, v104, 60, v146
	s_mov_b64 exec, s[96:97]
	ds_write_b32 v136, v146
	s_mov_b64 exec, -1
	v_add_u32_e32 v147, 0x700c0, v145
	v_and_or_b32 v147, v105, 60, v147
	s_mov_b64 exec, s[98:99]
	ds_write_b32 v137, v147
	s_mov_b64 exec, -1
	s_waitcnt lgkmcnt(0)
	s_barrier
	s_add_i32 s53, s8, 7
	s_lshr_b32 s53, s53, 3
	v_lshlrev_b32_e32 v218, 4, v1
	v_lshlrev_b32_e32 v219, 3, v1
	v_mov_b32_e32 v223, 0x11540
	v_and_b32_e32 v221, 7, v1
	v_mov_b32_e32 v200, 0
	v_mov_b32_e32 v201, 0
	v_mov_b32_e32 v202, 0
	v_mov_b32_e32 v203, 0
	v_mov_b32_e32 v204, 0
	v_mov_b32_e32 v205, 0
	v_mov_b32_e32 v206, 0
	v_mov_b32_e32 v207, 0
	s_mov_b32 s50, -1
	s_mov_b64 exec, 1
	ds_add_rtn_u32 v222, v223, v142
	s_mov_b64 exec, -1
	s_waitcnt lgkmcnt(0)
	v_readfirstlane_b32 s54, v222
	s_mov_b64 exec, 1
	ds_add_rtn_u32 v222, v223, v142
	s_mov_b64 exec, -1
	s_waitcnt lgkmcnt(0)
	v_readfirstlane_b32 s55, v222
	s_cmp_ge_u32 s54, s53
	s_cbranch_scc1 .Lg_nochunk
	s_lshl_b32 s46, s54, 3
	v_add_u32_e32 v220, s46, v221
	v_cmp_gt_u32_e32 vcc, s8, v220
	v_lshlrev_b32_e32 v220, 2, v220
	ds_read_b32 v216, v220
	s_waitcnt lgkmcnt(0)
	v_cndmask_b32_e32 v216, 1, v216, vcc
	s_nop 1
	v_readlane_b32 s50, v216, 0
	s_bfe_u32 s50, s50, 0x40002
	v_readlane_b32 s40, v216, 0
	s_bfe_u32 s60, s40, 0x40002
	s_bitcmp1_b32 s40, 0
	s_cselect_b32 s60, 16, s60
	s_and_b32 s40, s40, 0xffffffc0
	s_lshl_b32 s40, s40, 4
	s_add_u32 s42, s32, s40
	s_addc_u32 s43, s33, 0
	global_load_dwordx4 v[66:69], v218, s[42:43] nt
	v_readlane_b32 s40, v216, 1
	s_bfe_u32 s61, s40, 0x40002
	s_bitcmp1_b32 s40, 0
	s_cselect_b32 s61, 16, s61
	s_and_b32 s40, s40, 0xffffffc0
	s_lshl_b32 s40, s40, 4
	s_add_u32 s42, s32, s40
	s_addc_u32 s43, s33, 0
	global_load_dwordx4 v[70:73], v218, s[42:43] nt
	v_readlane_b32 s40, v216, 2
	s_bfe_u32 s62, s40, 0x40002
	s_bitcmp1_b32 s40, 0
	s_cselect_b32 s62, 16, s62
	s_and_b32 s40, s40, 0xffffffc0
	s_lshl_b32 s40, s40, 4
	s_add_u32 s42, s32, s40
	s_addc_u32 s43, s33, 0
	global_load_dwordx4 v[74:77], v218, s[42:43] nt
	v_readlane_b32 s40, v216, 3
	s_bfe_u32 s63, s40, 0x40002
	s_bitcmp1_b32 s40, 0
	s_cselect_b32 s63, 16, s63
	s_and_b32 s40, s40, 0xffffffc0
	s_lshl_b32 s40, s40, 4
	s_add_u32 s42, s32, s40
	s_addc_u32 s43, s33, 0
	global_load_dwordx4 v[78:81], v218, s[42:43] nt
	v_readlane_b32 s40, v216, 4
	s_bfe_u32 s64, s40, 0x40002
	s_bitcmp1_b32 s40, 0
	s_cselect_b32 s64, 16, s64
	s_and_b32 s40, s40, 0xffffffc0
	s_lshl_b32 s40, s40, 4
	s_add_u32 s42, s32, s40
	s_addc_u32 s43, s33, 0
	global_load_dwordx4 v[82:85], v218, s[42:43] nt
	v_readlane_b32 s40, v216, 5
	s_bfe_u32 s65, s40, 0x40002
	s_bitcmp1_b32 s40, 0
	s_cselect_b32 s65, 16, s65
	s_and_b32 s40, s40, 0xffffffc0
	s_lshl_b32 s40, s40, 4
	s_add_u32 s42, s32, s40
	s_addc_u32 s43, s33, 0
	global_load_dwordx4 v[86:89], v218, s[42:43] nt
	v_readlane_b32 s40, v216, 6
	s_bfe_u32 s66, s40, 0x40002
	s_bitcmp1_b32 s40, 0
	s_cselect_b32 s66, 16, s66
	s_and_b32 s40, s40, 0xffffffc0
	s_lshl_b32 s40, s40, 4
	s_add_u32 s42, s32, s40
	s_addc_u32 s43, s33, 0
	global_load_dwordx4 v[90:93], v218, s[42:43] nt
	v_readlane_b32 s40, v216, 7
	s_bfe_u32 s67, s40, 0x40002
	s_bitcmp1_b32 s40, 0
	s_cselect_b32 s67, 16, s67
	s_and_b32 s40, s40, 0xffffffc0
	s_lshl_b32 s40, s40, 4
	s_add_u32 s42, s32, s40
	s_addc_u32 s43, s33, 0
	global_load_dwordx4 v[94:97], v218, s[42:43] nt
	s_cmp_ge_u32 s55, s53
	s_cbranch_scc1 .Lg_noB
	s_lshl_b32 s46, s55, 3
	v_add_u32_e32 v220, s46, v221
	v_cmp_gt_u32_e32 vcc, s8, v220
	v_lshlrev_b32_e32 v220, 2, v220
	ds_read_b32 v217, v220
	s_waitcnt lgkmcnt(0)
	v_cndmask_b32_e32 v217, 1, v217, vcc
	s_nop 1
	v_readlane_b32 s40, v217, 0
	s_bfe_u32 s68, s40, 0x40002
	s_bitcmp1_b32 s40, 0
	s_cselect_b32 s68, 16, s68
	s_and_b32 s40, s40, 0xffffffc0
	s_lshl_b32 s40, s40, 4
	s_add_u32 s42, s32, s40
	s_addc_u32 s43, s33, 0
	global_load_dwordx4 v[98:101], v218, s[42:43] nt
	v_readlane_b32 s40, v217, 1
	s_bfe_u32 s69, s40, 0x40002
	s_bitcmp1_b32 s40, 0
	s_cselect_b32 s69, 16, s69
	s_and_b32 s40, s40, 0xffffffc0
	s_lshl_b32 s40, s40, 4
	s_add_u32 s42, s32, s40
	s_addc_u32 s43, s33, 0
	global_load_dwordx4 v[102:105], v218, s[42:43] nt
	v_readlane_b32 s40, v217, 2
	s_bfe_u32 s70, s40, 0x40002
	s_bitcmp1_b32 s40, 0
	s_cselect_b32 s70, 16, s70
	s_and_b32 s40, s40, 0xffffffc0
	s_lshl_b32 s40, s40, 4
	s_add_u32 s42, s32, s40
	s_addc_u32 s43, s33, 0
	global_load_dwordx4 v[106:109], v218, s[42:43] nt
	v_readlane_b32 s40, v217, 3
	s_bfe_u32 s71, s40, 0x40002
	s_bitcmp1_b32 s40, 0
	s_cselect_b32 s71, 16, s71
	s_and_b32 s40, s40, 0xffffffc0
	s_lshl_b32 s40, s40, 4
	s_add_u32 s42, s32, s40
	s_addc_u32 s43, s33, 0
	global_load_dwordx4 v[110:113], v218, s[42:43] nt
	v_readlane_b32 s40, v217, 4
	s_bfe_u32 s72, s40, 0x40002
	s_bitcmp1_b32 s40, 0
	s_cselect_b32 s72, 16, s72
	s_and_b32 s40, s40, 0xffffffc0
	s_lshl_b32 s40, s40, 4
	s_add_u32 s42, s32, s40
	s_addc_u32 s43, s33, 0
	global_load_dwordx4 v[114:117], v218, s[42:43] nt
	v_readlane_b32 s40, v217, 5
	s_bfe_u32 s73, s40, 0x40002
	s_bitcmp1_b32 s40, 0
	s_cselect_b32 s73, 16, s73
	s_and_b32 s40, s40, 0xffffffc0
	s_lshl_b32 s40, s40, 4
	s_add_u32 s42, s32, s40
	s_addc_u32 s43, s33, 0
	global_load_dwordx4 v[118:121], v218, s[42:43] nt
	v_readlane_b32 s40, v217, 6
	s_bfe_u32 s74, s40, 0x40002
	s_bitcmp1_b32 s40, 0
	s_cselect_b32 s74, 16, s74
	s_and_b32 s40, s40, 0xffffffc0
	s_lshl_b32 s40, s40, 4
	s_add_u32 s42, s32, s40
	s_addc_u32 s43, s33, 0
	global_load_dwordx4 v[122:125], v218, s[42:43] nt
	v_readlane_b32 s40, v217, 7
	s_bfe_u32 s75, s40, 0x40002
	s_bitcmp1_b32 s40, 0
	s_cselect_b32 s75, 16, s75
	s_and_b32 s40, s40, 0xffffffc0
	s_lshl_b32 s40, s40, 4
	s_add_u32 s42, s32, s40
	s_addc_u32 s43, s33, 0
	global_load_dwordx4 v[126:129], v218, s[42:43] nt
	s_waitcnt vmcnt(16)
	v_mul_f32_e32 v150, v62, v62
	v_mul_f32_e32 v151, v63, v63
	v_mul_f32_e32 v152, v64, v64
	v_mul_f32_e32 v153, v65, v65
	v_fmac_f32_e32 v150, v58, v58
	v_fmac_f32_e32 v151, v59, v59
	v_fmac_f32_e32 v152, v60, v60
	v_fmac_f32_e32 v153, v61, v61
	v_fmac_f32_e32 v150, v54, v54
	v_fmac_f32_e32 v151, v55, v55
	v_fmac_f32_e32 v152, v56, v56
	v_fmac_f32_e32 v153, v57, v57
	v_fmac_f32_e32 v150, v50, v50
	v_fmac_f32_e32 v151, v51, v51
	v_fmac_f32_e32 v152, v52, v52
	v_fmac_f32_e32 v153, v53, v53
	v_fmac_f32_e32 v150, v46, v46
	v_fmac_f32_e32 v151, v47, v47
	v_fmac_f32_e32 v152, v48, v48
	v_fmac_f32_e32 v153, v49, v49
	v_fmac_f32_e32 v150, v42, v42
	v_fmac_f32_e32 v151, v43, v43
	v_fmac_f32_e32 v152, v44, v44
	v_fmac_f32_e32 v153, v45, v45
	v_fmac_f32_e32 v150, v38, v38
	v_fmac_f32_e32 v151, v39, v39
	v_fmac_f32_e32 v152, v40, v40
	v_fmac_f32_e32 v153, v41, v41
	v_fmac_f32_e32 v150, v34, v34
	v_fmac_f32_e32 v151, v35, v35
	v_fmac_f32_e32 v152, v36, v36
	v_fmac_f32_e32 v153, v37, v37
	v_fmac_f32_e32 v150, v30, v30
	v_fmac_f32_e32 v151, v31, v31
	v_fmac_f32_e32 v152, v32, v32
	v_fmac_f32_e32 v153, v33, v33
	v_fmac_f32_e32 v150, v26, v26
	v_fmac_f32_e32 v151, v27, v27
	v_fmac_f32_e32 v152, v28, v28
	v_fmac_f32_e32 v153, v29, v29
	v_fmac_f32_e32 v150, v22, v22
	v_fmac_f32_e32 v151, v23, v23
	v_fmac_f32_e32 v152, v24, v24
	v_fmac_f32_e32 v153, v25, v25
	v_fmac_f32_e32 v150, v18, v18
	v_fmac_f32_e32 v151, v19, v19
	v_fmac_f32_e32 v152, v20, v20
	v_fmac_f32_e32 v153, v21, v21
	v_fmac_f32_e32 v150, v14, v14
	v_fmac_f32_e32 v151, v15, v15
	v_fmac_f32_e32 v152, v16, v16
	v_fmac_f32_e32 v153, v17, v17
	v_fmac_f32_e32 v150, v10, v10
	v_fmac_f32_e32 v151, v11, v11
	v_fmac_f32_e32 v152, v12, v12
	v_fmac_f32_e32 v153, v13, v13
	v_fmac_f32_e32 v150, v6, v6
	v_fmac_f32_e32 v151, v7, v7
	v_fmac_f32_e32 v152, v8, v8
	v_fmac_f32_e32 v153, v9, v9
	v_fmac_f32_e32 v150, v2, v2
	v_fmac_f32_e32 v151, v3, v3
	v_fmac_f32_e32 v152, v4, v4
	v_fmac_f32_e32 v153, v5, v5
	v_add_f32_e32 v150, v150, v151
	v_add_f32_e32 v152, v152, v153
	v_add_f32_e32 v150, v150, v152
	v_mbcnt_lo_u32_b32 v151, -1, 0
	v_mbcnt_hi_u32_b32 v151, -1, v151
	v_xor_b32_e32 v152, 16, v151
	v_lshlrev_b32_e32 v152, 2, v152
	ds_bpermute_b32 v152, v152, v150
	v_xor_b32_e32 v153, 32, v151
	v_lshlrev_b32_e32 v153, 2, v153
	s_waitcnt lgkmcnt(0)
	v_add_f32_e32 v150, v150, v152
	ds_bpermute_b32 v153, v153, v150
	v_add_u32_e32 v152, s24, v1
	v_lshlrev_b32_e32 v152, 2, v152
	v_add_u32_e32 v152, 0x11300, v152
	v_cmp_gt_u32_e32 vcc, 16, v1
	s_and_saveexec_b64 s[30:31], vcc
	s_waitcnt lgkmcnt(0)
	v_add_f32_e32 v150, v150, v153
	ds_write_b32 v152, v150
	s_mov_b64 exec, s[30:31]

.Lg_noB:
	s_waitcnt vmcnt(16)
	v_mul_f32_e32 v150, v62, v62
	v_mul_f32_e32 v151, v63, v63
	v_mul_f32_e32 v152, v64, v64
	v_mul_f32_e32 v153, v65, v65
	v_fmac_f32_e32 v150, v58, v58
	v_fmac_f32_e32 v151, v59, v59
	v_fmac_f32_e32 v152, v60, v60
	v_fmac_f32_e32 v153, v61, v61
	v_fmac_f32_e32 v150, v54, v54
	v_fmac_f32_e32 v151, v55, v55
	v_fmac_f32_e32 v152, v56, v56
	v_fmac_f32_e32 v153, v57, v57
	v_fmac_f32_e32 v150, v50, v50
	v_fmac_f32_e32 v151, v51, v51
	v_fmac_f32_e32 v152, v52, v52
	v_fmac_f32_e32 v153, v53, v53
	v_fmac_f32_e32 v150, v46, v46
	v_fmac_f32_e32 v151, v47, v47
	v_fmac_f32_e32 v152, v48, v48
	v_fmac_f32_e32 v153, v49, v49
	v_fmac_f32_e32 v150, v42, v42
	v_fmac_f32_e32 v151, v43, v43
	v_fmac_f32_e32 v152, v44, v44
	v_fmac_f32_e32 v153, v45, v45
	v_fmac_f32_e32 v150, v38, v38
	v_fmac_f32_e32 v151, v39, v39
	v_fmac_f32_e32 v152, v40, v40
	v_fmac_f32_e32 v153, v41, v41
	v_fmac_f32_e32 v150, v34, v34
	v_fmac_f32_e32 v151, v35, v35
	v_fmac_f32_e32 v152, v36, v36
	v_fmac_f32_e32 v153, v37, v37
	v_fmac_f32_e32 v150, v30, v30
	v_fmac_f32_e32 v151, v31, v31
	v_fmac_f32_e32 v152, v32, v32
	v_fmac_f32_e32 v153, v33, v33
	v_fmac_f32_e32 v150, v26, v26
	v_fmac_f32_e32 v151, v27, v27
	v_fmac_f32_e32 v152, v28, v28
	v_fmac_f32_e32 v153, v29, v29
	v_fmac_f32_e32 v150, v22, v22
	v_fmac_f32_e32 v151, v23, v23
	v_fmac_f32_e32 v152, v24, v24
	v_fmac_f32_e32 v153, v25, v25
	v_fmac_f32_e32 v150, v18, v18
	v_fmac_f32_e32 v151, v19, v19
	v_fmac_f32_e32 v152, v20, v20
	v_fmac_f32_e32 v153, v21, v21
	v_fmac_f32_e32 v150, v14, v14
	v_fmac_f32_e32 v151, v15, v15
	v_fmac_f32_e32 v152, v16, v16
	v_fmac_f32_e32 v153, v17, v17
	v_fmac_f32_e32 v150, v10, v10
	v_fmac_f32_e32 v151, v11, v11
	v_fmac_f32_e32 v152, v12, v12
	v_fmac_f32_e32 v153, v13, v13
	v_fmac_f32_e32 v150, v6, v6
	v_fmac_f32_e32 v151, v7, v7
	v_fmac_f32_e32 v152, v8, v8
	v_fmac_f32_e32 v153, v9, v9
	v_fmac_f32_e32 v150, v2, v2
	v_fmac_f32_e32 v151, v3, v3
	v_fmac_f32_e32 v152, v4, v4
	v_fmac_f32_e32 v153, v5, v5
	v_add_f32_e32 v150, v150, v151
	v_add_f32_e32 v152, v152, v153
	v_add_f32_e32 v150, v150, v152
	v_mbcnt_lo_u32_b32 v151, -1, 0
	v_mbcnt_hi_u32_b32 v151, -1, v151
	v_xor_b32_e32 v152, 16, v151
	v_lshlrev_b32_e32 v152, 2, v152
	ds_bpermute_b32 v152, v152, v150
	v_xor_b32_e32 v153, 32, v151
	v_lshlrev_b32_e32 v153, 2, v153
	s_waitcnt lgkmcnt(0)
	v_add_f32_e32 v150, v150, v152
	ds_bpermute_b32 v153, v153, v150
	v_add_u32_e32 v152, s24, v1
	v_lshlrev_b32_e32 v152, 2, v152
	v_add_u32_e32 v152, 0x11300, v152
	v_cmp_gt_u32_e32 vcc, 16, v1
	s_and_saveexec_b64 s[30:31], vcc
	s_waitcnt lgkmcnt(0)
	v_add_f32_e32 v150, v150, v153
	ds_write_b32 v152, v150
	s_mov_b64 exec, s[30:31]

.Lg_nochunk:
	s_waitcnt vmcnt(16)
	v_mul_f32_e32 v150, v62, v62
	v_mul_f32_e32 v151, v63, v63
	v_mul_f32_e32 v152, v64, v64
	v_mul_f32_e32 v153, v65, v65
	v_fmac_f32_e32 v150, v58, v58
	v_fmac_f32_e32 v151, v59, v59
	v_fmac_f32_e32 v152, v60, v60
	v_fmac_f32_e32 v153, v61, v61
	v_fmac_f32_e32 v150, v54, v54
	v_fmac_f32_e32 v151, v55, v55
	v_fmac_f32_e32 v152, v56, v56
	v_fmac_f32_e32 v153, v57, v57
	v_fmac_f32_e32 v150, v50, v50
	v_fmac_f32_e32 v151, v51, v51
	v_fmac_f32_e32 v152, v52, v52
	v_fmac_f32_e32 v153, v53, v53
	v_fmac_f32_e32 v150, v46, v46
	v_fmac_f32_e32 v151, v47, v47
	v_fmac_f32_e32 v152, v48, v48
	v_fmac_f32_e32 v153, v49, v49
	v_fmac_f32_e32 v150, v42, v42
	v_fmac_f32_e32 v151, v43, v43
	v_fmac_f32_e32 v152, v44, v44
	v_fmac_f32_e32 v153, v45, v45
	v_fmac_f32_e32 v150, v38, v38
	v_fmac_f32_e32 v151, v39, v39
	v_fmac_f32_e32 v152, v40, v40
	v_fmac_f32_e32 v153, v41, v41
	v_fmac_f32_e32 v150, v34, v34
	v_fmac_f32_e32 v151, v35, v35
	v_fmac_f32_e32 v152, v36, v36
	v_fmac_f32_e32 v153, v37, v37
	v_fmac_f32_e32 v150, v30, v30
	v_fmac_f32_e32 v151, v31, v31
	v_fmac_f32_e32 v152, v32, v32
	v_fmac_f32_e32 v153, v33, v33
	v_fmac_f32_e32 v150, v26, v26
	v_fmac_f32_e32 v151, v27, v27
	v_fmac_f32_e32 v152, v28, v28
	v_fmac_f32_e32 v153, v29, v29
	v_fmac_f32_e32 v150, v22, v22
	v_fmac_f32_e32 v151, v23, v23
	v_fmac_f32_e32 v152, v24, v24
	v_fmac_f32_e32 v153, v25, v25
	v_fmac_f32_e32 v150, v18, v18
	v_fmac_f32_e32 v151, v19, v19
	v_fmac_f32_e32 v152, v20, v20
	v_fmac_f32_e32 v153, v21, v21
	v_fmac_f32_e32 v150, v14, v14
	v_fmac_f32_e32 v151, v15, v15
	v_fmac_f32_e32 v152, v16, v16
	v_fmac_f32_e32 v153, v17, v17
	v_fmac_f32_e32 v150, v10, v10
	v_fmac_f32_e32 v151, v11, v11
	v_fmac_f32_e32 v152, v12, v12
	v_fmac_f32_e32 v153, v13, v13
	v_fmac_f32_e32 v150, v6, v6
	v_fmac_f32_e32 v151, v7, v7
	v_fmac_f32_e32 v152, v8, v8
	v_fmac_f32_e32 v153, v9, v9
	v_fmac_f32_e32 v150, v2, v2
	v_fmac_f32_e32 v151, v3, v3
	v_fmac_f32_e32 v152, v4, v4
	v_fmac_f32_e32 v153, v5, v5
	v_add_f32_e32 v150, v150, v151
	v_add_f32_e32 v152, v152, v153
	v_add_f32_e32 v150, v150, v152
	v_mbcnt_lo_u32_b32 v151, -1, 0
	v_mbcnt_hi_u32_b32 v151, -1, v151
	v_xor_b32_e32 v152, 16, v151
	v_lshlrev_b32_e32 v152, 2, v152
	ds_bpermute_b32 v152, v152, v150
	v_xor_b32_e32 v153, 32, v151
	v_lshlrev_b32_e32 v153, 2, v153
	s_waitcnt lgkmcnt(0)
	v_add_f32_e32 v150, v150, v152
	ds_bpermute_b32 v153, v153, v150
	v_add_u32_e32 v152, s24, v1
	v_lshlrev_b32_e32 v152, 2, v152
	v_add_u32_e32 v152, 0x11300, v152
	v_cmp_gt_u32_e32 vcc, 16, v1
	s_and_saveexec_b64 s[30:31], vcc
	s_waitcnt lgkmcnt(0)
	v_add_f32_e32 v150, v150, v153
	ds_write_b32 v152, v150
	s_mov_b64 exec, s[30:31]
	s_branch .Lg_alldone

.LBB0_118:
	s_waitcnt vmcnt(0)
	v_lshrrev_b32_e32 v67, 4, v0
	v_mov_b32_e32 v66, 0x11100
	v_lshl_or_b32 v66, v67, 2, v66
	s_waitcnt lgkmcnt(0)
	s_barrier
	ds_read_b32 v66, v66
	v_mul_u32_u24_e32 v68, 0x102, v67
	v_lshlrev_b32_e32 v72, 3, v68
	s_waitcnt lgkmcnt(0)
	v_max_i32_e32 v66, 1, v66
	v_cvt_f32_u32_e32 v66, v66
	v_div_scale_f32 v69, s[0:1], v66, v66, 1.0
	v_rcp_f32_e32 v70, v69
	v_div_scale_f32 v68, vcc, 1.0, v66, 1.0
	v_fma_f32 v71, -v69, v70, 1.0
	v_fmac_f32_e32 v70, v71, v70
	v_mul_f32_e32 v71, v68, v70
	v_fma_f32 v73, -v69, v71, v68
	v_fmac_f32_e32 v71, v73, v70
	v_fma_f32 v68, -v69, v71, v68
	v_div_fmas_f32 v73, v68, v70, v71
	v_lshl_add_u32 v68, v138, 3, v72
	v_add_u32_e32 v76, 0x8000, v68
	ds_read2_b64 v[68:71], v76 offset1:16
	v_div_fixup_f32 v77, v73, v66, 1.0
	v_mul_i32_i24_e32 v73, 0xfffffbf8, v67
	v_lshlrev_b32_e32 v66, 2, v138
	v_add3_u32 v78, v72, v73, v66
	ds_read2_b64 v[72:75], v76 offset0:32 offset1:48
	s_waitcnt lgkmcnt(1)
	v_cvt_f32_f64_e32 v68, v[68:69]
	v_cvt_f32_f64_e32 v69, v[70:71]
	v_mul_f32_e32 v68, v77, v68
	v_mul_f32_e32 v69, v77, v69
	v_fma_f32 v79, v68, v68, 0
	ds_write2_b32 v78, v68, v69 offset1:16
	s_waitcnt lgkmcnt(1)
	v_cvt_f32_f64_e32 v68, v[72:73]
	v_fmac_f32_e32 v79, v69, v69
	v_mul_f32_e32 v72, v77, v68
	ds_read2_b64 v[68:71], v76 offset0:64 offset1:80
	v_cvt_f32_f64_e32 v73, v[74:75]
	v_fmac_f32_e32 v79, v72, v72
	v_mul_f32_e32 v73, v77, v73
	v_fmac_f32_e32 v79, v73, v73
	ds_write2_b32 v78, v72, v73 offset0:32 offset1:48
	ds_read2_b64 v[72:75], v76 offset0:96 offset1:112
	s_waitcnt lgkmcnt(2)
	v_cvt_f32_f64_e32 v68, v[68:69]
	v_cvt_f32_f64_e32 v69, v[70:71]
	v_mul_f32_e32 v68, v77, v68
	v_mul_f32_e32 v69, v77, v69
	v_fmac_f32_e32 v79, v68, v68
	ds_write2_b32 v78, v68, v69 offset0:64 offset1:80
	s_waitcnt lgkmcnt(1)
	v_cvt_f32_f64_e32 v68, v[72:73]
	v_fmac_f32_e32 v79, v69, v69
	v_mul_f32_e32 v72, v77, v68
	ds_read2_b64 v[68:71], v76 offset0:128 offset1:144
	v_cvt_f32_f64_e32 v73, v[74:75]
	v_fmac_f32_e32 v79, v72, v72
	v_mul_f32_e32 v73, v77, v73
	v_fmac_f32_e32 v79, v73, v73
	ds_write2_b32 v78, v72, v73 offset0:96 offset1:112
	ds_read2_b64 v[72:75], v76 offset0:160 offset1:176
	s_waitcnt lgkmcnt(2)
	v_cvt_f32_f64_e32 v68, v[68:69]
	v_cvt_f32_f64_e32 v69, v[70:71]
	v_mul_f32_e32 v68, v77, v68
	v_mul_f32_e32 v69, v77, v69
	v_fmac_f32_e32 v79, v68, v68
	ds_write2_b32 v78, v68, v69 offset0:128 offset1:144
	s_waitcnt lgkmcnt(1)
	v_cvt_f32_f64_e32 v68, v[72:73]
	v_fmac_f32_e32 v79, v69, v69
	v_mul_f32_e32 v72, v77, v68
	ds_read2_b64 v[68:71], v76 offset0:192 offset1:208
	v_cvt_f32_f64_e32 v73, v[74:75]
	v_fmac_f32_e32 v79, v72, v72
	v_mul_f32_e32 v73, v77, v73
	v_fmac_f32_e32 v79, v73, v73
	ds_write2_b32 v78, v72, v73 offset0:160 offset1:176
	ds_read2_b64 v[72:75], v76 offset0:224 offset1:240
	s_waitcnt lgkmcnt(2)
	v_cvt_f32_f64_e32 v68, v[68:69]
	v_cvt_f32_f64_e32 v69, v[70:71]
	v_mul_f32_e32 v68, v77, v68
	v_mul_f32_e32 v69, v77, v69
	v_fmac_f32_e32 v79, v68, v68
	ds_write2_b32 v78, v68, v69 offset0:192 offset1:208
	s_waitcnt lgkmcnt(1)
	v_cvt_f32_f64_e32 v68, v[72:73]
	v_fmac_f32_e32 v79, v69, v69
	v_mul_f32_e32 v68, v77, v68
	v_cvt_f32_f64_e32 v69, v[74:75]
	v_fmac_f32_e32 v79, v68, v68
	v_mul_f32_e32 v69, v77, v69
	v_fmac_f32_e32 v79, v69, v69
	ds_write2_b32 v78, v68, v69 offset0:224 offset1:240
	v_cmp_eq_u32_e32 vcc, 0, v138
	v_add_f32_dpp v68, v79, v79 quad_perm:[1,0,3,2] row_mask:0xf bank_mask:0xf bound_ctrl:1
	s_nop 1
	v_add_f32_dpp v68, v68, v68 quad_perm:[2,3,0,1] row_mask:0xf bank_mask:0xf bound_ctrl:1
	s_nop 1
	v_add_f32_dpp v68, v68, v68 row_half_mirror row_mask:0xf bank_mask:0xf bound_ctrl:1
	s_nop 1
	v_mov_b32_dpp v69, v68 row_mirror row_mask:0xf bank_mask:0xf bound_ctrl:1
	s_and_saveexec_b64 s[0:1], vcc
	v_mov_b32_e32 v70, 0x11200
	v_lshl_or_b32 v67, v67, 2, v70
	v_add_f32_e32 v68, v68, v69
	ds_write_b32 v67, v68
	s_or_b64 exec, exec, s[0:1]
	v_lshlrev_b32_e32 v67, 2, v140
	s_movk_i32 s0, 0x408
	v_mad_u32_u24 v67, v138, s0, v67
	s_waitcnt lgkmcnt(0)
	s_barrier
	ds_read2_b32 v[68:69], v67 offset1:4
	ds_read2_b32 v[70:71], v67 offset0:64 offset1:68
	ds_read2_b32 v[72:73], v67 offset0:192 offset1:196
	s_lshl_b32 s29, s17, 2
	s_lshl_b32 s0, s24, 2
	s_waitcnt lgkmcnt(2)
	v_mfma_f32_16x16x4_f32 a[0:3], v68, v62, 0
	s_add_i32 s0, s0, 0x10100
	s_waitcnt lgkmcnt(1)
	v_mfma_f32_16x16x4_f32 a[0:3], v70, v63, a[0:3]
	ds_read2_b32 v[62:63], v67 offset0:128 offset1:132
	s_waitcnt lgkmcnt(0)
	v_mfma_f32_16x16x4_f32 a[0:3], v62, v64, a[0:3]
	v_mfma_f32_16x16x4_f32 a[0:3], v72, v65, a[0:3]
	v_mfma_f32_16x16x4_f32 a[0:3], v69, v58, a[0:3]
	v_mfma_f32_16x16x4_f32 a[0:3], v71, v59, a[0:3]
	ds_read2_b32 v[58:59], v67 offset0:8 offset1:12
	v_mfma_f32_16x16x4_f32 a[0:3], v63, v60, a[0:3]
	ds_read2_b32 v[62:63], v67 offset0:200 offset1:204
	v_mfma_f32_16x16x4_f32 a[0:3], v73, v61, a[0:3]
	ds_read2_b32 v[60:61], v67 offset0:72 offset1:76
	s_waitcnt lgkmcnt(2)
	v_mfma_f32_16x16x4_f32 a[0:3], v58, v54, a[0:3]
	s_waitcnt lgkmcnt(0)
	v_mfma_f32_16x16x4_f32 a[0:3], v60, v55, a[0:3]
	ds_read2_b32 v[54:55], v67 offset0:136 offset1:140
	s_waitcnt lgkmcnt(0)
	v_mfma_f32_16x16x4_f32 a[0:3], v54, v56, a[0:3]
	v_mfma_f32_16x16x4_f32 a[0:3], v62, v57, a[0:3]
	v_mfma_f32_16x16x4_f32 a[0:3], v59, v50, a[0:3]
	v_mfma_f32_16x16x4_f32 a[0:3], v61, v51, a[0:3]
	ds_read2_b32 v[50:51], v67 offset0:16 offset1:20
	v_mfma_f32_16x16x4_f32 a[0:3], v55, v52, a[0:3]
	ds_read2_b32 v[54:55], v67 offset0:208 offset1:212
	v_mfma_f32_16x16x4_f32 a[0:3], v63, v53, a[0:3]
	ds_read2_b32 v[52:53], v67 offset0:80 offset1:84
	s_waitcnt lgkmcnt(2)
	v_mfma_f32_16x16x4_f32 a[0:3], v50, v46, a[0:3]
	s_waitcnt lgkmcnt(0)
	v_mfma_f32_16x16x4_f32 a[0:3], v52, v47, a[0:3]
	ds_read2_b32 v[46:47], v67 offset0:144 offset1:148
	s_waitcnt lgkmcnt(0)
	v_mfma_f32_16x16x4_f32 a[0:3], v46, v48, a[0:3]
	v_mfma_f32_16x16x4_f32 a[0:3], v54, v49, a[0:3]
	v_mfma_f32_16x16x4_f32 a[0:3], v51, v42, a[0:3]
	v_mfma_f32_16x16x4_f32 a[0:3], v53, v43, a[0:3]
	ds_read2_b32 v[42:43], v67 offset0:24 offset1:28
	v_mfma_f32_16x16x4_f32 a[0:3], v47, v44, a[0:3]
	ds_read2_b32 v[46:47], v67 offset0:216 offset1:220
	v_mfma_f32_16x16x4_f32 a[0:3], v55, v45, a[0:3]
	ds_read2_b32 v[44:45], v67 offset0:88 offset1:92
	s_waitcnt lgkmcnt(2)
	v_mfma_f32_16x16x4_f32 a[0:3], v42, v38, a[0:3]
	s_waitcnt lgkmcnt(0)
	v_mfma_f32_16x16x4_f32 a[0:3], v44, v39, a[0:3]
	ds_read2_b32 v[38:39], v67 offset0:152 offset1:156
	s_waitcnt lgkmcnt(0)
	v_mfma_f32_16x16x4_f32 a[0:3], v38, v40, a[0:3]
	v_mfma_f32_16x16x4_f32 a[0:3], v46, v41, a[0:3]
	v_mfma_f32_16x16x4_f32 a[0:3], v43, v34, a[0:3]
	v_mfma_f32_16x16x4_f32 a[0:3], v45, v35, a[0:3]
	ds_read2_b32 v[34:35], v67 offset0:32 offset1:36
	v_mfma_f32_16x16x4_f32 a[0:3], v39, v36, a[0:3]
	ds_read2_b32 v[38:39], v67 offset0:224 offset1:228
	v_mfma_f32_16x16x4_f32 a[0:3], v47, v37, a[0:3]
	ds_read2_b32 v[36:37], v67 offset0:96 offset1:100
	s_waitcnt lgkmcnt(2)
	v_mfma_f32_16x16x4_f32 a[0:3], v34, v30, a[0:3]
	s_waitcnt lgkmcnt(0)
	v_mfma_f32_16x16x4_f32 a[0:3], v36, v31, a[0:3]
	ds_read2_b32 v[30:31], v67 offset0:160 offset1:164
	s_waitcnt lgkmcnt(0)
	v_mfma_f32_16x16x4_f32 a[0:3], v30, v32, a[0:3]
	v_mfma_f32_16x16x4_f32 a[0:3], v38, v33, a[0:3]
	v_mfma_f32_16x16x4_f32 a[0:3], v35, v26, a[0:3]
	v_mfma_f32_16x16x4_f32 a[0:3], v37, v27, a[0:3]
	ds_read2_b32 v[26:27], v67 offset0:40 offset1:44
	v_mfma_f32_16x16x4_f32 a[0:3], v31, v28, a[0:3]
	ds_read2_b32 v[30:31], v67 offset0:232 offset1:236
	v_mfma_f32_16x16x4_f32 a[0:3], v39, v29, a[0:3]
	ds_read2_b32 v[28:29], v67 offset0:104 offset1:108
	s_waitcnt lgkmcnt(2)
	v_mfma_f32_16x16x4_f32 a[0:3], v26, v22, a[0:3]
	s_waitcnt lgkmcnt(0)
	v_mfma_f32_16x16x4_f32 a[0:3], v28, v23, a[0:3]
	ds_read2_b32 v[22:23], v67 offset0:168 offset1:172
	s_waitcnt lgkmcnt(0)
	v_mfma_f32_16x16x4_f32 a[0:3], v22, v24, a[0:3]
	v_mfma_f32_16x16x4_f32 a[0:3], v30, v25, a[0:3]
	v_mfma_f32_16x16x4_f32 a[0:3], v27, v18, a[0:3]
	v_mfma_f32_16x16x4_f32 a[0:3], v29, v19, a[0:3]
	ds_read2_b32 v[18:19], v67 offset0:48 offset1:52
	v_mfma_f32_16x16x4_f32 a[0:3], v23, v20, a[0:3]
	ds_read2_b32 v[22:23], v67 offset0:240 offset1:244
	v_mfma_f32_16x16x4_f32 a[0:3], v31, v21, a[0:3]
	ds_read2_b32 v[20:21], v67 offset0:112 offset1:116
	s_waitcnt lgkmcnt(2)
	v_mfma_f32_16x16x4_f32 a[0:3], v18, v14, a[0:3]
	s_waitcnt lgkmcnt(0)
	v_mfma_f32_16x16x4_f32 a[0:3], v20, v15, a[0:3]
	ds_read2_b32 v[14:15], v67 offset0:176 offset1:180
	s_waitcnt lgkmcnt(0)
	v_mfma_f32_16x16x4_f32 a[0:3], v14, v16, a[0:3]
	v_mfma_f32_16x16x4_f32 a[0:3], v22, v17, a[0:3]
	v_mfma_f32_16x16x4_f32 a[0:3], v19, v10, a[0:3]
	v_mfma_f32_16x16x4_f32 a[0:3], v21, v11, a[0:3]
	ds_read2_b32 v[10:11], v67 offset0:56 offset1:60
	v_mfma_f32_16x16x4_f32 a[0:3], v15, v12, a[0:3]
	ds_read2_b32 v[14:15], v67 offset0:248 offset1:252
	v_mfma_f32_16x16x4_f32 a[0:3], v23, v13, a[0:3]
	ds_read2_b32 v[12:13], v67 offset0:120 offset1:124
	s_waitcnt lgkmcnt(2)
	v_mfma_f32_16x16x4_f32 a[0:3], v10, v6, a[0:3]
	s_waitcnt lgkmcnt(0)
	v_mfma_f32_16x16x4_f32 a[0:3], v12, v7, a[0:3]
	ds_read2_b32 v[6:7], v67 offset0:184 offset1:188
	s_waitcnt lgkmcnt(0)
	v_mfma_f32_16x16x4_f32 a[0:3], v6, v8, a[0:3]
	v_mfma_f32_16x16x4_f32 a[0:3], v14, v9, a[0:3]
	v_mfma_f32_16x16x4_f32 a[0:3], v11, v2, a[0:3]
	v_mov_b32_e32 v2, 0x11300
	v_lshl_add_u32 v2, v134, 2, v2
	ds_read_b32 v2, v2
	v_mfma_f32_16x16x4_f32 a[0:3], v13, v3, a[0:3]
	v_lshlrev_b32_e32 v3, 10, v140
	v_add3_u32 v3, s0, v66, v3
	v_mfma_f32_16x16x4_f32 a[0:3], v7, v4, a[0:3]
	v_or_b32_e32 v7, s29, v140
	v_lshl_or_b32 v4, v7, 8, v66
	v_add_u32_e32 v4, 0x10100, v4
	v_mfma_f32_16x16x4_f32 a[0:3], v15, v5, a[0:3]
	s_nop 9
	v_accvgpr_read_b32 v5, a0
	v_accvgpr_read_b32 v6, a1
	v_accvgpr_read_b32 v8, a2
	v_accvgpr_read_b32 v9, a3
	s_waitcnt lgkmcnt(0)
	v_fma_f32 v5, -2.0, v5, v2
	v_fma_f32 v6, -2.0, v6, v2
	v_fma_f32 v8, -2.0, v8, v2
	v_fmac_f32_e32 v2, -2.0, v9
	ds_write2st64_b32 v3, v5, v6 offset1:1
	ds_write2st64_b32 v3, v8, v2 offset0:2 offset1:3
	s_waitcnt lgkmcnt(0)
	s_barrier
	ds_read2_b32 v[2:3], v4 offset1:16
	ds_read2_b32 v[4:5], v4 offset0:32 offset1:48
	v_or_b32_e32 v6, 16, v138
	v_or_b32_e32 v8, 32, v138
	v_or_b32_e32 v9, 48, v138
	s_waitcnt lgkmcnt(1)
	v_cmp_lt_f32_e32 vcc, v3, v2
	s_nop 1
	v_cndmask_b32_e32 v10, v2, v3, vcc
	v_cndmask_b32_e32 v6, v138, v6, vcc
	s_waitcnt lgkmcnt(0)
	v_cmp_lt_f32_e32 vcc, v4, v10
	s_nop 1
	v_cndmask_b32_e32 v10, v10, v4, vcc
	v_cndmask_b32_e32 v8, v6, v8, vcc
	v_cmp_lt_f32_e32 vcc, v5, v10
	s_nop 1
	v_cndmask_b32_e32 v6, v10, v5, vcc
	v_cndmask_b32_e32 v14, v8, v9, vcc
	s_nop 0
	v_mov_b32_dpp v9, v6 quad_perm:[1,0,3,2] row_mask:0xf bank_mask:0xf bound_ctrl:1
	v_mov_b32_dpp v8, v14 quad_perm:[1,0,3,2] row_mask:0xf bank_mask:0xf bound_ctrl:1
	v_cmp_gt_f32_e64 s[4:5], v6, v9
	v_cmp_ngt_f32_e32 vcc, v6, v9
	s_and_saveexec_b64 s[6:7], vcc
	v_cmp_eq_f32_e32 vcc, v6, v9
	v_cmp_lt_i32_e64 s[0:1], v8, v14
	s_and_b64 s[0:1], vcc, s[0:1]
	s_andn2_b64 s[4:5], s[4:5], exec
	s_and_b64 s[0:1], s[0:1], exec
	s_or_b64 s[4:5], s[4:5], s[0:1]
	s_or_b64 exec, exec, s[6:7]
	s_and_saveexec_b64 s[0:1], s[4:5]
	v_mov_b32_e32 v6, v9
	v_mov_b32_e32 v14, v8
	s_or_b64 exec, exec, s[0:1]
	v_mov_b32_dpp v9, v6 quad_perm:[2,3,0,1] row_mask:0xf bank_mask:0xf bound_ctrl:1
	v_mov_b32_dpp v8, v14 quad_perm:[2,3,0,1] row_mask:0xf bank_mask:0xf bound_ctrl:1
	v_cmp_gt_f32_e64 s[4:5], v6, v9
	v_cmp_ngt_f32_e32 vcc, v6, v9
	s_and_saveexec_b64 s[6:7], vcc
	v_cmp_eq_f32_e32 vcc, v6, v9
	v_cmp_lt_i32_e64 s[0:1], v8, v14
	s_and_b64 s[0:1], vcc, s[0:1]
	s_andn2_b64 s[4:5], s[4:5], exec
	s_and_b64 s[0:1], s[0:1], exec
	s_or_b64 s[4:5], s[4:5], s[0:1]
	s_or_b64 exec, exec, s[6:7]
	s_and_saveexec_b64 s[0:1], s[4:5]
	v_mov_b32_e32 v6, v9
	v_mov_b32_e32 v14, v8
	s_or_b64 exec, exec, s[0:1]
	v_mov_b32_dpp v9, v6 row_half_mirror row_mask:0xf bank_mask:0xf bound_ctrl:1
	v_mov_b32_dpp v8, v14 row_half_mirror row_mask:0xf bank_mask:0xf bound_ctrl:1
	v_cmp_gt_f32_e64 s[4:5], v6, v9
	v_cmp_ngt_f32_e32 vcc, v6, v9
	s_and_saveexec_b64 s[6:7], vcc
	v_cmp_eq_f32_e32 vcc, v6, v9
	v_cmp_lt_i32_e64 s[0:1], v8, v14
	s_and_b64 s[0:1], vcc, s[0:1]
	s_andn2_b64 s[4:5], s[4:5], exec
	s_and_b64 s[0:1], s[0:1], exec
	s_or_b64 s[4:5], s[4:5], s[0:1]
	s_or_b64 exec, exec, s[6:7]
	s_and_saveexec_b64 s[0:1], s[4:5]
	v_mov_b32_e32 v6, v9
	v_mov_b32_e32 v14, v8
	s_or_b64 exec, exec, s[0:1]
	v_mov_b32_dpp v8, v6 row_mirror row_mask:0xf bank_mask:0xf bound_ctrl:1
	v_mov_b32_dpp v9, v14 row_mirror row_mask:0xf bank_mask:0xf bound_ctrl:1
	v_cmp_gt_f32_e64 s[4:5], v6, v8
	v_cmp_ngt_f32_e32 vcc, v6, v8
	s_and_saveexec_b64 s[6:7], vcc
	v_cmp_eq_f32_e32 vcc, v6, v8
	v_cmp_lt_i32_e64 s[0:1], v9, v14
	s_and_b64 s[0:1], vcc, s[0:1]
	s_andn2_b64 s[4:5], s[4:5], exec
	s_and_b64 s[0:1], s[0:1], exec
	s_or_b64 s[4:5], s[4:5], s[0:1]
	s_or_b64 exec, exec, s[6:7]
	s_and_saveexec_b64 s[0:1], s[4:5]
	v_mov_b32_e32 v6, v8
	v_mov_b32_e32 v14, v9
	s_or_b64 exec, exec, s[0:1]
	v_lshlrev_b32_e32 v86, 2, v139
	v_readlane_b32 s92, v14, 0
	v_readlane_b32 s93, v14, 16
	v_readlane_b32 s94, v14, 32
	v_readlane_b32 s95, v14, 48
	s_lshl_b32 s96, s92, 10
	s_add_u32 s96, s22, s96
	s_addc_u32 s97, s23, 0
	global_load_dwordx4 v[70:73], v86, s[96:97]
	s_lshl_b32 s96, s93, 10
	s_add_u32 s96, s22, s96
	s_addc_u32 s97, s23, 0
	global_load_dwordx4 v[74:77], v86, s[96:97]
	s_lshl_b32 s96, s94, 10
	s_add_u32 s96, s22, s96
	s_addc_u32 s97, s23, 0
	global_load_dwordx4 v[78:81], v86, s[96:97]
	s_lshl_b32 s96, s95, 10
	s_add_u32 s96, s22, s96
	s_addc_u32 s97, s23, 0
	global_load_dwordx4 v[82:85], v86, s[96:97]
	v_mov_b32_e32 v8, 0x11300
	v_lshl_or_b32 v8, v1, 2, v8
	ds_read_b32 v8, v8
	v_mov_b32_e32 v9, 0x11200
	v_lshl_add_u32 v7, v7, 2, v9
	ds_read_b32 v9, v7
	v_mov_b32_e32 v13, 0x260
	s_waitcnt lgkmcnt(1)
	v_mov_b32_dpp v7, v8 quad_perm:[1,0,3,2] row_mask:0xf bank_mask:0xf bound_ctrl:1
	v_max_f32_e32 v8, v8, v8
	v_max_f32_e32 v7, v7, v7
	v_max_f32_e32 v7, v8, v7
	v_lshlrev_b32_e32 v18, 2, v139
	v_mov_b32_e32 v19, 0
	v_mov_b32_dpp v8, v7 quad_perm:[2,3,0,1] row_mask:0xf bank_mask:0xf bound_ctrl:1
	v_max_f32_e32 v8, v8, v8
	v_max_f32_e32 v7, v7, v8
	s_mov_b32 s25, 0
	s_mov_b32 s26, s25
	v_mov_b32_dpp v8, v7 row_half_mirror row_mask:0xf bank_mask:0xf bound_ctrl:1
	v_max_f32_e32 v8, v8, v8
	v_max_f32_e32 v7, v7, v8
	s_nop 1
	v_mov_b32_dpp v8, v7 row_mirror row_mask:0xf bank_mask:0xf bound_ctrl:1
	v_max_f32_e32 v8, v8, v8
	v_max_f32_e32 v7, v7, v8
	s_nop 0
	v_readlane_b32 s4, v7, 32
	v_readlane_b32 s5, v7, 48
	v_readlane_b32 s0, v7, 0
	v_readlane_b32 s1, v7, 16
	v_max_f32_e64 v7, s5, s5
	v_max_f32_e64 v8, s4, s4
	v_max_f32_e32 v7, v8, v7
	v_mov_b32_e32 v8, s1
	v_max3_f32 v8, s0, v8, v7
	s_mov_b32 s0, 0x3f800347
	s_mov_b32 s1, 0x3f8020c5
	s_waitcnt lgkmcnt(0)
	v_pk_mul_f32 v[8:9], v[8:9], s[0:1]
	s_mov_b32 s4, 0xf800000
	v_mul_f32_e32 v7, 0x4f800000, v9
	v_cmp_gt_f32_e32 vcc, s4, v9
	s_nop 1
	v_cndmask_b32_e32 v7, v9, v7, vcc
	v_sqrt_f32_e32 v10, v7
	s_nop 0
	v_add_u32_e32 v11, -1, v10
	v_fma_f32 v12, -v11, v10, v7
	v_cmp_ge_f32_e64 s[0:1], 0, v12
	v_add_u32_e32 v12, 1, v10
	s_nop 0
	v_cndmask_b32_e64 v11, v10, v11, s[0:1]
	v_fma_f32 v10, -v12, v10, v7
	v_cmp_lt_f32_e64 s[0:1], 0, v10
	s_nop 1
	v_cndmask_b32_e64 v10, v11, v12, s[0:1]
	v_mul_f32_e32 v11, 0x37800000, v10
	v_cndmask_b32_e32 v10, v10, v11, vcc
	v_mul_f32_e32 v11, 0x4f800000, v8
	v_cmp_gt_f32_e32 vcc, s4, v8
	v_cmp_class_f32_e64 s[0:1], v7, v13
	s_nop 0
	v_cndmask_b32_e32 v11, v8, v11, vcc
	v_sqrt_f32_e32 v12, v11
	v_cndmask_b32_e64 v7, v10, v7, s[0:1]
	v_add_u32_e32 v10, -1, v12
	v_fma_f32 v15, -v10, v12, v11
	v_cmp_ge_f32_e64 s[0:1], 0, v15
	v_add_u32_e32 v15, 1, v12
	s_nop 0
	v_cndmask_b32_e64 v10, v12, v10, s[0:1]
	v_fma_f32 v12, -v15, v12, v11
	v_cmp_lt_f32_e64 s[0:1], 0, v12
	s_nop 1
	v_cndmask_b32_e64 v10, v10, v15, s[0:1]
	v_mul_f32_e32 v12, 0x37800000, v10
	v_cndmask_b32_e32 v10, v10, v12, vcc
	v_cmp_class_f32_e32 vcc, v11, v13
	s_mov_b32 s0, 0x380637bd
	s_mov_b32 s1, 0x350637bd
	v_cndmask_b32_e32 v10, v10, v11, vcc
	v_mul_f32_e32 v7, v7, v10
	v_mul_f32_e32 v7, 0x3f800347, v7
	v_pk_mul_f32 v[8:9], v[8:9], s[0:1]
	s_nop 0
	v_fmamk_f32 v7, v7, 0x3888509c, v9
	v_add_f32_e32 v7, v8, v7
	v_add_f32_e32 v7, 0xda24260, v7
	v_add_f32_e32 v6, v6, v7
	v_cmp_le_f32_e64 s[8:9], v2, v6
	v_cmp_le_f32_e64 s[6:7], v3, v6
	v_cmp_le_f32_e64 s[4:5], v4, v6
	v_lshl_add_u64 v[2:3], s[22:23], 0, v[18:19]
	s_and_b32 s19, s8, 0xffff
	s_lshl_b32 s22, s6, 16
	v_cmp_le_f32_e64 s[0:1], v5, v6
	s_or_b32 s24, s19, s22
	s_and_b32 s23, s4, 0xffff
	s_mov_b32 s22, s25
	s_or_b64 s[22:23], s[24:25], s[22:23]
	s_lshl_b32 s27, s0, 16
	s_or_b64 s[26:27], s[22:23], s[26:27]
	s_add_u32 s22, s26, -1
	s_addc_u32 s23, s27, -1
	s_and_b64 s[22:23], s[26:27], s[22:23]
	s_cmp_eq_u64 s[22:23], 0
	v_readlane_b32 s22, v14, 0
	s_cbranch_scc1 .LBB0_139
	s_lshl_b32 s19, s29, 2
	s_add_i32 s19, s19, 0x11100
	v_mov_b32_e32 v4, s19
	ds_read_b32 v4, v4
	s_mul_i32 s19, s17, 0x2040
	v_add_u32_e32 v8, s19, v135
	v_mov_b32_e32 v15, 0x7f800000
	s_waitcnt lgkmcnt(0)
	v_max_i32_e32 v4, 1, v4
	v_cvt_f64_u32_e32 v[12:13], v4
	v_div_scale_f64 v[16:17], s[30:31], v[12:13], v[12:13], 1.0
	v_rcp_f64_e32 v[20:21], v[16:17]
	v_div_scale_f64 v[22:23], vcc, 1.0, v[12:13], 1.0
	ds_read2st64_b64 v[4:7], v8 offset0:64 offset1:65
	ds_read2st64_b64 v[8:11], v8 offset0:66 offset1:67
	v_fma_f64 v[24:25], -v[16:17], v[20:21], 1.0
	v_fmac_f64_e32 v[20:21], v[20:21], v[24:25]
	v_fma_f64 v[24:25], -v[16:17], v[20:21], 1.0
	v_fmac_f64_e32 v[20:21], v[20:21], v[24:25]
	v_mul_f64 v[24:25], v[22:23], v[20:21]
	v_fma_f64 v[16:17], -v[16:17], v[24:25], v[22:23]
	v_div_fmas_f64 v[16:17], v[16:17], v[20:21], v[24:25]
	v_div_fixup_f64 v[12:13], v[16:17], v[12:13], 1.0
	s_waitcnt lgkmcnt(1)
	v_mul_f64 v[6:7], v[6:7], v[12:13]
	v_mul_f64 v[4:5], v[4:5], v[12:13]
	s_waitcnt lgkmcnt(0)
	v_mul_f64 v[8:9], v[8:9], v[12:13]
	v_mul_f64 v[10:11], v[12:13], v[10:11]
	v_mul_f64 v[12:13], v[6:7], v[6:7]
	v_fmac_f64_e32 v[12:13], v[4:5], v[4:5]
	v_fmac_f64_e32 v[12:13], v[8:9], v[8:9]
	v_fmac_f64_e32 v[12:13], v[10:11], v[10:11]
	s_nop 1
	v_mov_b32_dpp v16, v12 quad_perm:[1,0,3,2] row_mask:0xf bank_mask:0xf bound_ctrl:1
	v_mov_b32_dpp v17, v13 quad_perm:[1,0,3,2] row_mask:0xf bank_mask:0xf bound_ctrl:1
	v_add_f64 v[12:13], v[12:13], v[16:17]
	s_nop 1
	v_mov_b32_dpp v16, v12 quad_perm:[2,3,0,1] row_mask:0xf bank_mask:0xf bound_ctrl:1
	v_mov_b32_dpp v17, v13 quad_perm:[2,3,0,1] row_mask:0xf bank_mask:0xf bound_ctrl:1
	v_add_f64 v[12:13], v[12:13], v[16:17]
	s_nop 1
	v_mov_b32_dpp v16, v12 row_half_mirror row_mask:0xf bank_mask:0xf bound_ctrl:1
	v_mov_b32_dpp v17, v13 row_half_mirror row_mask:0xf bank_mask:0xf bound_ctrl:1
	v_add_f64 v[12:13], v[12:13], v[16:17]
	s_nop 1
	v_mov_b32_dpp v16, v12 row_mirror row_mask:0xf bank_mask:0xf bound_ctrl:1
	v_mov_b32_dpp v17, v13 row_mirror row_mask:0xf bank_mask:0xf bound_ctrl:1
	v_add_f64 v[12:13], v[12:13], v[16:17]
	s_nop 0
	v_readlane_b32 s19, v13, 16
	v_readlane_b32 s23, v12, 16
	v_readlane_b32 s31, v13, 0
	v_readlane_b32 s30, v12, 0
	v_mov_b32_e32 v16, s23
	v_mov_b32_e32 v17, s19
	v_readlane_b32 s19, v13, 48
	v_readlane_b32 s23, v12, 48
	v_add_f64 v[16:17], s[30:31], v[16:17]
	v_readlane_b32 s31, v13, 32
	v_readlane_b32 s30, v12, 32
	v_mov_b32_e32 v12, s23
	v_mov_b32_e32 v13, s19
	v_add_f64 v[12:13], s[30:31], v[12:13]
	v_add_f64 v[12:13], v[16:17], v[12:13]

.LBB0_148:
	s_cmp_lg_u32 s22, s92
	s_cbranch_scc1 .Lpf_miss
	s_cmp_lg_u32 s8, s93
	s_cbranch_scc1 .Lpf_miss
	s_cmp_lg_u32 s0, s94
	s_cbranch_scc1 .Lpf_miss
	s_cmp_lg_u32 s4, s95
	s_cbranch_scc1 .Lpf_miss
	s_waitcnt vmcnt(0)
	v_mov_b64_e32 v[14:15], v[70:71]
	v_mov_b64_e32 v[16:17], v[72:73]
	v_mov_b64_e32 v[10:11], v[74:75]
	v_mov_b64_e32 v[12:13], v[76:77]
	v_mov_b64_e32 v[6:7], v[78:79]
	v_mov_b64_e32 v[8:9], v[80:81]
	v_mov_b64_e32 v[2:3], v[82:83]
	v_mov_b64_e32 v[4:5], v[84:85]
	s_branch .Lpf_join

.Lpf_join:
	s_mul_i32 s1, s17, 0x1020
	v_mov_b32_e32 v19, 0
	v_lshl_add_u32 v1, v1, 2, s1
	v_lshl_add_u64 v[20:21], s[20:21], 0, v[18:19]
	v_add_u32_e32 v18, 8, v1
	v_add_u32_e32 v22, 16, v1
	ds_read2st64_b32 v[36:37], v1 offset1:1
	ds_read2st64_b32 v[34:35], v1 offset0:2 offset1:3
	v_add_u32_e32 v1, 24, v1
	ds_read2st64_b32 v[32:33], v18 offset0:4 offset1:5
	ds_read2st64_b32 v[30:31], v18 offset0:6 offset1:7
	ds_read2st64_b32 v[28:29], v22 offset0:8 offset1:9
	ds_read2st64_b32 v[26:27], v22 offset0:10 offset1:11
	ds_read2st64_b32 v[24:25], v1 offset0:12 offset1:13
	ds_read2st64_b32 v[22:23], v1 offset0:14 offset1:15
	s_lshl_b32 s5, s18, 9
	s_or_b32 s1, s5, s28
	s_waitcnt lgkmcnt(7)
	v_add_f32_e64 v1, |v36|, |v37|
	s_mov_b32 s7, 0
	s_add_i32 s6, s1, s29
	s_waitcnt lgkmcnt(6)
	v_add_f32_e64 v1, |v34|, v1
	s_lshl_b64 s[18:19], s[6:7], 10
	v_add_f32_e64 v1, |v35|, v1
	v_lshl_add_u64 v[42:43], v[20:21], 0, s[18:19]
	v_cmp_lt_f32_e32 vcc, 0, v1
	s_waitcnt vmcnt(3)
	v_pk_add_f32 v[38:39], v[14:15], v[36:37] neg_lo:[0,1] neg_hi:[0,1]
	v_pk_add_f32 v[40:41], v[16:17], v[34:35] neg_lo:[0,1] neg_hi:[0,1]
	v_pk_add_f32 v[38:39], v[36:37], v[38:39]
	v_pk_add_f32 v[40:41], v[34:35], v[40:41]
	global_store_dwordx4 v[42:43], v[38:41], off nt
	s_cbranch_vccz .LBB0_150
	v_pk_add_f32 v[14:15], v[36:37], v[14:15] neg_lo:[0,1] neg_hi:[0,1]
	v_pk_add_f32 v[16:17], v[34:35], v[16:17] neg_lo:[0,1] neg_hi:[0,1]
	v_pk_mul_f32 v[14:15], v[14:15], v[14:15]
	v_pk_mul_f32 v[16:17], v[16:17], v[16:17]
	v_add_f32_e32 v1, v14, v15
	v_add_f32_e32 v1, v1, v16
	v_add_f32_e32 v19, v1, v17
	s_mov_b32 s7, 1
